# baseline (speedup 1.0000x reference)
.LBB2_16:
	v_add_u32_e32 v110, 0, v195
	v_add_u32_e32 v118, 0, v196
	ds_read_b128 v[82:85], v193 offset:8192
	ds_read_b128 v[86:89], v193 offset:9216
	ds_read_b128 v[90:93], v110 offset:16384
	ds_read_b128 v[98:101], v110 offset:18432
	ds_read_b128 v[94:97], v118 offset:16384
	ds_read_b128 v[102:105], v118 offset:18432
	ds_read_b128 v[106:109], v110 offset:20480
	ds_read_b128 v[114:117], v110 offset:22528
	ds_read_b128 v[110:113], v118 offset:20480
	ds_read_b128 v[118:121], v118 offset:22528
	s_waitcnt lgkmcnt(0)
	v_mfma_f32_32x32x64_f8f6f4 v[50:65], v[82:89], v[90:97], v[50:65]
	s_cmp_lg_u32 s39, 0
	s_cselect_b64 s[0:1], -1, 0
	v_cmp_eq_u32_e32 vcc, 0, v198
	s_and_b64 s[6:7], vcc, s[0:1]
	v_mfma_f32_32x32x64_f8f6f4 v[34:49], v[82:89], v[98:105], v[34:49]
	v_mfma_f32_32x32x64_f8f6f4 v[18:33], v[82:89], v[106:113], v[18:33]
	v_mfma_f32_32x32x64_f8f6f4 v[2:17], v[82:89], v[114:121], v[2:17]
	s_and_saveexec_b64 s[0:1], s[6:7]
	s_add_i32 s6, 0, 0x1cc00
	v_mov_b32_e32 v82, 1
	v_mov_b32_e32 v83, s6
	ds_write_b32 v83, v82
	s_or_b64 exec, exec, s[0:1]
	v_mov_b32_e32 v67, v66
	s_lshl_b32 s0, s34, 9
	s_lshl_b32 s1, s33, 2
	s_add_i32 s0, s0, 0x1c000
	v_permlane32_swap_b32_e32 v67, v66
	s_add_i32 s0, s0, s1
	v_lshl_add_u32 v68, v1, 2, s0
	v_add_f32_e32 v66, v66, v67
	ds_write_b32 v68, v66
	s_add_i32 s1, s1, 0x1c000
	v_lshl_add_u32 v69, v183, 4, s1
	s_add_i32 s0, 0, 0x1cc00
	v_mov_b32_e32 v82, s0
	s_waitcnt vmcnt(0) lgkmcnt(0)
	s_barrier
	ds_read_b32 v82, v82
	s_waitcnt lgkmcnt(0)
	v_cmp_eq_u32_e32 vcc, 0, v82
	s_cbranch_vccnz .Lat_lsum
	s_mov_b32 m0, s36
	s_barrier
	global_load_lds_dwordx4 v[174:175], off
	s_mov_b32 m0, s35
	s_lshl_b32 s0, s34, 5
	global_load_lds_dwordx4 v[176:177], off
	s_mov_b32 m0, s31
	s_lshl_b32 s1, s34, 7
	global_load_lds_dwordx4 v[178:179], off
	s_mov_b32 m0, s37
	s_add_i32 s1, s1, 0
	global_load_lds_dwordx4 v[180:181], off
	v_or_b32_e32 v2, s0, v1
	s_add_i32 s1, s1, 0x1c400
	v_bitop3_b32 v4, s0, 32, v1 bitop3:0x36
	v_lshlrev_b32_e32 v2, 2, v2
	v_add_u32_e32 v3, s1, v199
	v_lshlrev_b32_e32 v5, 4, v183
	v_lshlrev_b32_e32 v4, 2, v4
	v_add3_u32 v120, s38, v2, v199
	v_mov_b32_e32 v2, 0
	s_mov_b32 s20, 0
	v_lshl_add_u32 v118, v1, 2, v3
	v_add3_u32 v119, s38, v4, v199
	v_mov_b32_e32 v101, 0xf149f2ca
	s_mov_b64 s[0:1], 0
	s_mov_b64 s[6:7], 0x4000
	s_mov_b64 s[8:9], 0x6000
	v_add_u32_e32 v121, v3, v5
	s_mov_b32 s21, 0xbdb8aa3b
	v_mov_b32_e32 v82, 0x4b400000
	v_mov_b32_e32 v100, 0x38383838
	v_mov_b32_e32 v3, v2
	v_mov_b32_e32 v4, v2
	v_mov_b32_e32 v5, v2
	v_mov_b32_e32 v6, v2
	v_mov_b32_e32 v7, v2
	v_mov_b32_e32 v8, v2
	v_mov_b32_e32 v9, v2
	v_mov_b32_e32 v10, v2
	v_mov_b32_e32 v11, v2
	v_mov_b32_e32 v12, v2
	v_mov_b32_e32 v13, v2
	v_mov_b32_e32 v14, v2
	v_mov_b32_e32 v15, v2
	v_mov_b32_e32 v16, v2
	v_mov_b32_e32 v17, v2
	v_mov_b32_e32 v18, v2
	v_mov_b32_e32 v19, v2
	v_mov_b32_e32 v20, v2
	v_mov_b32_e32 v21, v2
	v_mov_b32_e32 v22, v2
	v_mov_b32_e32 v23, v2
	v_mov_b32_e32 v24, v2
	v_mov_b32_e32 v25, v2
	v_mov_b32_e32 v26, v2
	v_mov_b32_e32 v27, v2
	v_mov_b32_e32 v28, v2
	v_mov_b32_e32 v29, v2
	v_mov_b32_e32 v30, v2
	v_mov_b32_e32 v31, v2
	v_mov_b32_e32 v32, v2
	v_mov_b32_e32 v33, v2
	v_mov_b32_e32 v34, v2
	v_mov_b32_e32 v35, v2
	v_mov_b32_e32 v36, v2
	v_mov_b32_e32 v37, v2
	v_mov_b32_e32 v38, v2
	v_mov_b32_e32 v39, v2
	v_mov_b32_e32 v40, v2
	v_mov_b32_e32 v41, v2
	v_mov_b32_e32 v42, v2
	v_mov_b32_e32 v43, v2
	v_mov_b32_e32 v44, v2
	v_mov_b32_e32 v45, v2
	v_mov_b32_e32 v46, v2
	v_mov_b32_e32 v47, v2
	v_mov_b32_e32 v48, v2
	v_mov_b32_e32 v49, v2
	v_mov_b32_e32 v50, v2
	v_mov_b32_e32 v51, v2
	v_mov_b32_e32 v52, v2
	v_mov_b32_e32 v53, v2
	v_mov_b32_e32 v54, v2
	v_mov_b32_e32 v55, v2
	v_mov_b32_e32 v56, v2
	v_mov_b32_e32 v57, v2
	v_mov_b32_e32 v58, v2
	v_mov_b32_e32 v59, v2
	v_mov_b32_e32 v60, v2
	v_mov_b32_e32 v61, v2
	v_mov_b32_e32 v62, v2
	v_mov_b32_e32 v63, v2
	v_mov_b32_e32 v64, v2
	v_mov_b32_e32 v65, v2
	v_mov_b32_e32 v66, v2
	v_mov_b32_e32 v67, v2
	v_mov_b32_e32 v68, v2
	v_mov_b32_e32 v69, v2
	v_mov_b32_e32 v70, v2
	v_mov_b32_e32 v71, v2
	v_mov_b32_e32 v72, v2
	v_mov_b32_e32 v73, v2
	v_mov_b32_e32 v74, v2
	v_mov_b32_e32 v75, v2
	v_mov_b32_e32 v76, v2
	v_mov_b32_e32 v77, v2
	v_mov_b32_e32 v78, v2
	v_mov_b32_e32 v79, v2
	v_mov_b32_e32 v80, v2
	v_mov_b32_e32 v81, v2
	s_waitcnt vmcnt(0) lgkmcnt(0)
	s_barrier
	s_cmp_eq_u32 s0, 0x7c000
	s_movk_i32 s22, 0x4000
	s_cbranch_scc1 .LBB2_21

.Lat_lsum:
	ds_read_b128 v[70:73], v69
	ds_read_b128 v[74:77], v69 offset:32
	ds_read_b128 v[78:81], v69 offset:64
	ds_read_b128 v[82:85], v69 offset:96
	ds_read_b128 v[86:89], v69 offset:512
	ds_read_b128 v[90:93], v69 offset:544
	ds_read_b128 v[94:97], v69 offset:576
	ds_read_b128 v[98:101], v69 offset:608
	s_waitcnt lgkmcnt(0)
	v_add_f32_e32 v66, v70, v86
	v_add_f32_e32 v67, v71, v87
	v_add_f32_e32 v68, v72, v88
	v_add_f32_e32 v69, v73, v89
	v_add_f32_e32 v70, v74, v90
	v_add_f32_e32 v71, v75, v91
	v_add_f32_e32 v72, v76, v92
	v_add_f32_e32 v73, v77, v93
	v_add_f32_e32 v74, v78, v94
	v_add_f32_e32 v75, v79, v95
	v_add_f32_e32 v76, v80, v96
	v_add_f32_e32 v77, v81, v97
	v_add_f32_e32 v78, v82, v98
	v_add_f32_e32 v79, v83, v99
	v_add_f32_e32 v80, v84, v100
	v_add_f32_e32 v81, v85, v101
